# speedup vs baseline: 1.0146x; 1.0031x over previous
.Lstag_loop_p1:
	s_sleep 24
	s_add_i32 s20, s20, -1
	s_cmp_lg_u32 s20, 0
	s_cbranch_scc1 .Lstag_loop_p1
